# S10: S9 + K1 epilogue shuffle-tree levels xor8/4/2/1 via DPP (15 of 31 bpermutes removed, lgkmcnt waits re-derived)
# baseline (speedup 1.0000x reference)
.LBB0_2:
	s_or_b64 exec, exec, s[4:5]
	s_waitcnt lgkmcnt(0)
	s_barrier
	s_and_saveexec_b64 s[2:3], vcc
	s_cbranch_execz .LBB0_7
	v_lshl_or_b32 v38, v85, 13, v66
	ds_read2st64_b32 v[34:35], v38 offset1:1
	ds_read2st64_b32 v[36:37], v38 offset0:2 offset1:3
	ds_read2st64_b32 v[54:55], v38 offset0:6 offset1:7
	ds_read2st64_b32 v[56:57], v38 offset0:4 offset1:5
	ds_read2st64_b32 v[58:59], v38 offset0:8 offset1:9
	ds_read2st64_b32 v[60:61], v38 offset0:10 offset1:11
	ds_read2st64_b32 v[62:63], v38 offset0:12 offset1:13
	ds_read2st64_b32 v[64:65], v38 offset0:14 offset1:15
	s_load_dwordx2 s[2:3], s[0:1], 0x18
	ds_read2st64_b32 v[68:69], v38 offset0:16 offset1:17
	ds_read2st64_b32 v[52:53], v38 offset0:18 offset1:19
	ds_read2st64_b32 v[48:49], v38 offset0:20 offset1:21
	ds_read2st64_b32 v[50:51], v38 offset0:22 offset1:23
	ds_read2st64_b32 v[46:47], v38 offset0:24 offset1:25
	ds_read2st64_b32 v[44:45], v38 offset0:26 offset1:27
	ds_read2st64_b32 v[40:41], v38 offset0:28 offset1:29
	ds_read2st64_b32 v[42:43], v38 offset0:30 offset1:31
	s_waitcnt lgkmcnt(0)
	v_add_f32_e32 v66, v18, v34
	v_add_f32_e32 v58, v26, v58
	v_add_f32_e32 v26, v33, v65
	v_add_f32_e32 v65, v2, v68
	v_cvt_f16_f32_e32 v2, v66
	v_lshlrev_b32_e32 v38, 4, v84
	v_mov_b32_e32 v39, 0
	v_mov_b32_e32 v34, v35
	v_mov_b32_e32 v35, v36
	v_mov_b32_e32 v18, v19
	v_mov_b32_e32 v19, v20
	v_lshl_add_u64 v[72:73], s[2:3], 0, v[38:39]
	v_pk_add_f32 v[38:39], v[18:19], v[34:35]
	v_mov_b32_e32 v34, v37
	v_mov_b32_e32 v35, v56
	v_mov_b32_e32 v20, v21
	v_mov_b32_e32 v21, v22
	v_add_f32_e32 v46, v10, v46
	v_add_f32_e32 v10, v17, v43
	v_cvt_pk_f16_f32 v17, v38, v39
	v_pk_add_f32 v[34:35], v[20:21], v[34:35]
	v_add_f32_e32 v74, v25, v55
	v_pack_b32_f16 v18, v2, v17
	v_cvt_pk_f16_f32 v2, v34, v35
	v_add_f32_e32 v51, v9, v51
	v_ashrrev_i32_e32 v9, 4, v1
	s_mul_i32 s4, s8, 0xc0
	v_alignbit_b32 v19, v2, v17, 16
	v_cvt_f16_f32_e32 v17, v74
	v_add_u32_e32 v70, s4, v9
	v_mov_b32_e32 v20, v57
	v_mov_b32_e32 v21, v54
	v_mov_b32_e32 v22, v23
	v_mov_b32_e32 v23, v24
	v_pk_add_f32 v[36:37], v[22:23], v[20:21]
	v_ashrrev_i32_e32 v71, 31, v70
	v_cvt_pk_f16_f32 v21, v36, v37
	v_lshlrev_b64 v[22:23], 11, v[70:71]
	v_alignbit_b32 v20, v21, v2, 16
	v_alignbit_b32 v21, v17, v21, 16
	v_lshl_add_u64 v[54:55], v[72:73], 0, v[22:23]
	v_cvt_f16_f32_e32 v2, v58
	global_store_dwordx4 v[54:55], v[18:21], off
	v_mov_b32_e32 v22, v31
	v_mov_b32_e32 v23, v32
	v_mov_b32_e32 v18, v59
	v_mov_b32_e32 v19, v60
	v_mov_b32_e32 v20, v27
	v_mov_b32_e32 v21, v28
	v_pk_add_f32 v[24:25], v[20:21], v[18:19]
	v_mov_b32_e32 v18, v61
	v_mov_b32_e32 v19, v62
	v_mov_b32_e32 v20, v29
	v_mov_b32_e32 v21, v30
	v_cvt_pk_f16_f32 v17, v24, v25
	v_pk_add_f32 v[20:21], v[20:21], v[18:19]
	v_pack_b32_f16 v28, v2, v17
	v_cvt_pk_f16_f32 v2, v20, v21
	v_alignbit_b32 v29, v2, v17, 16
	v_cvt_f16_f32_e32 v17, v26
	v_mov_b32_e32 v18, v63
	v_mov_b32_e32 v19, v64
	v_pk_add_f32 v[22:23], v[22:23], v[18:19]
	s_nop 0
	v_cvt_pk_f16_f32 v18, v22, v23
	v_alignbit_b32 v30, v18, v2, 16
	v_alignbit_b32 v31, v17, v18, 16
	v_or_b32_e32 v18, 1, v70
	v_ashrrev_i32_e32 v19, 31, v18
	v_lshlrev_b64 v[18:19], 11, v[18:19]
	v_lshl_add_u64 v[18:19], v[72:73], 0, v[18:19]
	v_cvt_f16_f32_e32 v17, v65
	global_store_dwordx4 v[18:19], v[28:31], off
	v_mov_b32_e32 v2, v3
	v_mov_b32_e32 v3, v4
	v_mov_b32_e32 v28, v69
	v_mov_b32_e32 v29, v52
	v_mov_b32_e32 v30, v53
	v_mov_b32_e32 v31, v48
	v_mov_b32_e32 v4, v5
	v_mov_b32_e32 v5, v6
	v_mov_b32_e32 v6, v7
	v_mov_b32_e32 v7, v8
	v_cvt_f16_f32_e32 v8, v51
	v_pk_add_f32 v[28:29], v[2:3], v[28:29]
	v_pk_add_f32 v[30:31], v[4:5], v[30:31]
	v_mov_b32_e32 v4, v49
	v_mov_b32_e32 v5, v50
	v_cvt_pk_f16_f32 v3, v28, v29
	v_pk_add_f32 v[6:7], v[6:7], v[4:5]
	v_pack_b32_f16 v2, v17, v3
	v_cvt_pk_f16_f32 v17, v30, v31
	v_cvt_pk_f16_f32 v5, v6, v7
	v_alignbit_b32 v3, v17, v3, 16
	v_alignbit_b32 v4, v5, v17, 16
	v_alignbit_b32 v5, v8, v5, 16
	global_store_dwordx4 v[54:55], v[2:5], off offset:1024
	v_cvt_f16_f32_e32 v8, v46
	v_mul_f32_e32 v17, v82, v28
	v_mov_b32_e32 v2, v47
	v_mov_b32_e32 v3, v44
	v_mov_b32_e32 v4, v11
	v_mov_b32_e32 v5, v12
	v_pk_add_f32 v[32:33], v[4:5], v[2:3]
	v_mov_b32_e32 v5, v40
	v_mov_b32_e32 v12, v13
	v_mov_b32_e32 v13, v14
	v_mov_b32_e32 v40, v41
	v_mov_b32_e32 v41, v42
	v_mov_b32_e32 v14, v15
	v_mov_b32_e32 v15, v16
	v_mbcnt_lo_u32_b32 v42, -1, 0
	v_cvt_pk_f16_f32 v3, v32, v33
	v_mov_b32_e32 v4, v45
	v_pk_add_f32 v[14:15], v[14:15], v[40:41]
	v_mul_f32_e32 v41, v83, v32
	v_mul_f32_e32 v32, v82, v32
	v_mbcnt_hi_u32_b32 v42, -1, v42
	v_pk_add_f32 v[12:13], v[12:13], v[4:5]
	v_fmac_f32_e32 v41, v80, v24
	v_fmac_f32_e32 v32, v81, v24
	v_mul_f32_e32 v24, v83, v33
	v_mul_f32_e32 v33, v82, v33
	v_and_b32_e32 v43, 64, v42
	v_cvt_pk_f16_f32 v4, v12, v13
	v_fmac_f32_e32 v24, v80, v25
	v_fmac_f32_e32 v33, v81, v25
	v_mul_f32_e32 v25, v83, v12
	v_mul_f32_e32 v12, v82, v12
	v_add_u32_e32 v43, 64, v43
	v_xor_b32_e32 v45, 16, v42
	v_pack_b32_f16 v2, v8, v3
	v_mul_f32_e32 v8, v83, v65
	v_mul_f32_e32 v11, v82, v65
	v_mul_f32_e32 v16, v83, v28
	v_fmac_f32_e32 v25, v80, v20
	v_fmac_f32_e32 v12, v81, v20
	v_mul_f32_e32 v20, v83, v13
	v_mul_f32_e32 v13, v82, v13
	v_and_b32_e32 v44, 16, v0
	v_cmp_lt_i32_e32 vcc, v45, v43
	v_cvt_pk_f16_f32 v5, v14, v15
	v_fmac_f32_e32 v8, v80, v66
	v_fmac_f32_e32 v11, v81, v66
	v_fmac_f32_e32 v16, v80, v38
	v_fmac_f32_e32 v17, v81, v38
	v_mul_f32_e32 v27, v83, v29
	v_mul_f32_e32 v28, v82, v29
	v_fmac_f32_e32 v20, v80, v21
	v_fmac_f32_e32 v13, v81, v21
	v_mul_f32_e32 v21, v83, v14
	v_mul_f32_e32 v14, v82, v14
	v_cndmask_b32_e32 v45, v42, v45, vcc
	v_cmp_eq_u32_e32 vcc, 0, v44
	v_fmac_f32_e32 v27, v80, v39
	v_fmac_f32_e32 v28, v81, v39
	v_mul_f32_e32 v29, v83, v30
	v_mul_f32_e32 v30, v82, v30
	v_fmac_f32_e32 v21, v80, v22
	v_fmac_f32_e32 v14, v81, v22
	v_mul_f32_e32 v22, v83, v15
	v_mul_f32_e32 v15, v82, v15
	v_lshlrev_b32_e32 v45, 2, v45
	v_cndmask_b32_e32 v44, v8, v11, vcc
	v_cndmask_b32_e32 v8, v11, v8, vcc
	v_cndmask_b32_e32 v11, v16, v17, vcc
	v_fmac_f32_e32 v29, v80, v34
	v_fmac_f32_e32 v30, v81, v34
	v_mul_f32_e32 v39, v83, v46
	v_mul_f32_e32 v40, v82, v46
	v_fmac_f32_e32 v22, v80, v23
	v_fmac_f32_e32 v15, v81, v23
	v_mul_f32_e32 v23, v83, v10
	v_mul_f32_e32 v46, v82, v10
	v_cndmask_b32_e32 v16, v17, v16, vcc
	ds_bpermute_b32 v11, v45, v11
	v_cndmask_b32_e32 v17, v27, v28, vcc
	v_fmac_f32_e32 v23, v80, v26
	v_fmac_f32_e32 v46, v81, v26
	ds_bpermute_b32 v17, v45, v17
	v_cndmask_b32_e32 v26, v29, v30, vcc
	ds_bpermute_b32 v26, v45, v26
	v_mul_f32_e32 v34, v83, v31
	v_mul_f32_e32 v31, v82, v31
	v_fmac_f32_e32 v34, v80, v35
	v_fmac_f32_e32 v31, v81, v35
	v_mul_f32_e32 v35, v83, v6
	v_mul_f32_e32 v6, v82, v6
	s_waitcnt lgkmcnt(2)
	v_add_f32_e32 v11, v16, v11
	v_cndmask_b32_e32 v16, v28, v27, vcc
	v_fmac_f32_e32 v35, v80, v36
	v_fmac_f32_e32 v6, v81, v36
	v_mul_f32_e32 v36, v83, v7
	v_mul_f32_e32 v7, v82, v7
	s_waitcnt lgkmcnt(1)
	v_add_f32_e32 v16, v16, v17
	v_cndmask_b32_e32 v17, v30, v29, vcc
	v_fmac_f32_e32 v36, v80, v37
	v_fmac_f32_e32 v7, v81, v37
	s_waitcnt lgkmcnt(0)
	v_add_f32_e32 v17, v17, v26
	v_cndmask_b32_e32 v26, v34, v31, vcc
	ds_bpermute_b32 v26, v45, v26
	v_cndmask_b32_e32 v29, v36, v7, vcc
	ds_bpermute_b32 v29, v45, v29
	v_mul_f32_e32 v37, v83, v51
	v_mul_f32_e32 v38, v82, v51
	v_fmac_f32_e32 v37, v80, v74
	v_fmac_f32_e32 v38, v81, v74
	v_cndmask_b32_e32 v27, v31, v34, vcc
	v_cndmask_b32_e32 v28, v35, v6, vcc
	v_fmac_f32_e32 v39, v80, v58
	v_fmac_f32_e32 v40, v81, v58
	ds_bpermute_b32 v28, v45, v28
	s_waitcnt lgkmcnt(2)
	v_add_f32_e32 v26, v27, v26
	v_cndmask_b32_e32 v7, v7, v36, vcc
	v_cndmask_b32_e32 v27, v37, v38, vcc
	s_waitcnt lgkmcnt(1)
	v_add_f32_e32 v7, v7, v29
	ds_bpermute_b32 v27, v45, v27
	v_cndmask_b32_e32 v29, v39, v40, vcc
	ds_bpermute_b32 v29, v45, v29
	v_cndmask_b32_e32 v6, v6, v35, vcc
	s_waitcnt lgkmcnt(2)
	v_add_f32_e32 v6, v6, v28
	v_cndmask_b32_e32 v28, v38, v37, vcc
	s_waitcnt lgkmcnt(1)
	v_add_f32_e32 v27, v28, v27
	v_cndmask_b32_e32 v28, v40, v39, vcc
	v_cndmask_b32_e32 v30, v41, v32, vcc
	s_waitcnt lgkmcnt(0)
	v_add_f32_e32 v28, v28, v29
	v_cndmask_b32_e32 v29, v32, v41, vcc
	v_cndmask_b32_e32 v32, v20, v13, vcc
	v_cndmask_b32_e32 v13, v13, v20, vcc
	v_cndmask_b32_e32 v20, v21, v14, vcc
	v_cndmask_b32_e32 v14, v14, v21, vcc
	v_cndmask_b32_e32 v21, v22, v15, vcc
	ds_bpermute_b32 v30, v45, v30
	ds_bpermute_b32 v20, v45, v20
	ds_bpermute_b32 v21, v45, v21
	ds_bpermute_b32 v44, v45, v44
	v_cndmask_b32_e32 v15, v15, v22, vcc
	v_xor_b32_e32 v22, 8, v42
	s_waitcnt lgkmcnt(3)
	v_add_f32_e32 v29, v29, v30
	v_cndmask_b32_e32 v30, v24, v33, vcc
	v_cndmask_b32_e32 v24, v33, v24, vcc
	v_cndmask_b32_e32 v31, v25, v12, vcc
	v_cndmask_b32_e32 v12, v12, v25, vcc
	v_cndmask_b32_e32 v25, v23, v46, vcc
	s_waitcnt lgkmcnt(2)
	v_add_f32_e32 v14, v14, v20
	s_waitcnt lgkmcnt(1)
	v_add_f32_e32 v15, v15, v21
	v_cndmask_b32_e32 v20, v46, v23, vcc
	v_and_b32_e32 v21, 8, v0
	v_cmp_lt_i32_e32 vcc, v22, v43
	s_waitcnt lgkmcnt(0)
	v_add_f32_e32 v8, v8, v44
	ds_bpermute_b32 v31, v45, v31
	v_cndmask_b32_e32 v22, v42, v22, vcc
	v_cmp_eq_u32_e32 vcc, 0, v21
	v_lshlrev_b32_e32 v22, 2, v22
	ds_bpermute_b32 v32, v45, v32
	v_cndmask_b32_e32 v21, v8, v28, vcc
	s_nop 1
	v_mov_b32_dpp v21, v21 row_ror:8 row_mask:0xf bank_mask:0xf
	v_cndmask_b32_e32 v23, v11, v29, vcc
	ds_bpermute_b32 v30, v45, v30
	s_nop 1
	v_mov_b32_dpp v23, v23 row_ror:8 row_mask:0xf bank_mask:0xf
	s_waitcnt lgkmcnt(2)
	v_add_f32_e32 v12, v12, v31
	ds_bpermute_b32 v25, v45, v25
	v_cndmask_b32_e32 v8, v28, v8, vcc
	s_waitcnt lgkmcnt(2)
	v_add_f32_e32 v13, v13, v32
	s_waitcnt lgkmcnt(2)
	v_add_f32_e32 v8, v8, v21
	v_cndmask_b32_e32 v21, v17, v12, vcc
	v_cndmask_b32_e32 v12, v12, v17, vcc
	s_nop 1
	v_mov_b32_dpp v17, v21 row_ror:8 row_mask:0xf bank_mask:0xf
	v_cndmask_b32_e32 v21, v26, v13, vcc
	v_cndmask_b32_e32 v11, v29, v11, vcc
	s_nop 1
	v_mov_b32_dpp v21, v21 row_ror:8 row_mask:0xf bank_mask:0xf
	s_waitcnt lgkmcnt(1)
	v_add_f32_e32 v24, v24, v30
	s_waitcnt lgkmcnt(1)
	v_add_f32_e32 v11, v11, v23
	v_cndmask_b32_e32 v23, v6, v14, vcc
	s_waitcnt lgkmcnt(0)
	v_add_f32_e32 v20, v20, v25
	v_cndmask_b32_e32 v25, v16, v24, vcc
	s_nop 1
	v_mov_b32_dpp v23, v23 row_ror:8 row_mask:0xf bank_mask:0xf
	v_cndmask_b32_e32 v6, v14, v6, vcc
	v_cndmask_b32_e32 v14, v7, v15, vcc
	s_nop 1
	v_mov_b32_dpp v25, v25 row_ror:8 row_mask:0xf bank_mask:0xf
	s_nop 1
	v_mov_b32_dpp v14, v14 row_ror:8 row_mask:0xf bank_mask:0xf
	v_cndmask_b32_e32 v13, v13, v26, vcc
	v_cndmask_b32_e32 v7, v15, v7, vcc
	v_cndmask_b32_e32 v15, v27, v20, vcc
	s_waitcnt lgkmcnt(0)
	v_add_f32_e32 v13, v13, v21
	s_nop 1
	v_mov_b32_dpp v15, v15 row_ror:8 row_mask:0xf bank_mask:0xf
	v_xor_b32_e32 v21, 4, v42
	v_add_f32_e32 v12, v12, v17
	v_and_b32_e32 v17, 4, v0
	v_cmp_lt_i32_e64 s[2:3], v21, v43
	v_cndmask_b32_e32 v16, v24, v16, vcc
	s_waitcnt lgkmcnt(0)
	v_add_f32_e32 v6, v6, v23
	v_cndmask_b32_e64 v21, v42, v21, s[2:3]
	v_cmp_eq_u32_e64 s[2:3], 0, v17
	s_waitcnt lgkmcnt(0)
	v_add_f32_e32 v16, v16, v25
	v_lshlrev_b32_e32 v21, 2, v21
	v_cndmask_b32_e64 v17, v8, v13, s[2:3]
	s_waitcnt lgkmcnt(0)
	v_add_f32_e32 v7, v7, v14
	v_cndmask_b32_e64 v8, v13, v8, s[2:3]
	v_cndmask_b32_e64 v13, v11, v6, s[2:3]
	v_cndmask_b32_e32 v14, v20, v27, vcc
	v_cndmask_b32_e64 v6, v6, v11, s[2:3]
	s_nop 1
	v_mov_b32_dpp v11, v13 row_half_mirror row_mask:0xf bank_mask:0xf
	s_nop 1
	v_mov_b32_dpp v11, v11 quad_perm:[3,2,1,0] row_mask:0xf bank_mask:0xf
	v_cndmask_b32_e64 v13, v16, v7, s[2:3]
	s_waitcnt lgkmcnt(0)
	v_add_f32_e32 v14, v14, v15
	s_nop 1
	v_mov_b32_dpp v13, v13 row_half_mirror row_mask:0xf bank_mask:0xf
	s_nop 1
	v_mov_b32_dpp v13, v13 quad_perm:[3,2,1,0] row_mask:0xf bank_mask:0xf
	v_cndmask_b32_e64 v15, v12, v14, s[2:3]
	s_nop 1
	v_mov_b32_dpp v17, v17 row_half_mirror row_mask:0xf bank_mask:0xf
	s_nop 1
	v_mov_b32_dpp v17, v17 quad_perm:[3,2,1,0] row_mask:0xf bank_mask:0xf
	s_nop 1
	v_mov_b32_dpp v15, v15 row_half_mirror row_mask:0xf bank_mask:0xf
	s_nop 1
	v_mov_b32_dpp v15, v15 quad_perm:[3,2,1,0] row_mask:0xf bank_mask:0xf
	v_cndmask_b32_e64 v7, v7, v16, s[2:3]
	s_waitcnt lgkmcnt(0)
	v_add_f32_e32 v7, v7, v13
	v_xor_b32_e32 v13, 2, v42
	v_add_f32_e32 v6, v6, v11
	v_cndmask_b32_e64 v11, v14, v12, s[2:3]
	v_and_b32_e32 v12, 2, v0
	v_cmp_lt_i32_e32 vcc, v13, v43
	s_waitcnt lgkmcnt(0)
	v_add_f32_e32 v8, v8, v17
	s_waitcnt lgkmcnt(0)
	v_add_f32_e32 v11, v11, v15
	v_cndmask_b32_e32 v13, v42, v13, vcc
	v_cmp_eq_u32_e32 vcc, 0, v12
	v_lshlrev_b32_e32 v13, 2, v13
	v_cvt_f16_f32_e32 v10, v10
	v_cndmask_b32_e32 v12, v8, v7, vcc
	v_cndmask_b32_e32 v14, v6, v11, vcc
	s_nop 1
	v_mov_b32_dpp v12, v12 quad_perm:[2,3,0,1] row_mask:0xf bank_mask:0xf
	s_nop 1
	v_mov_b32_dpp v13, v14 quad_perm:[2,3,0,1] row_mask:0xf bank_mask:0xf
	v_cndmask_b32_e32 v6, v11, v6, vcc
	v_xor_b32_e32 v11, 1, v42
	v_cndmask_b32_e32 v7, v7, v8, vcc
	v_and_b32_e32 v8, 1, v0
	v_cmp_lt_i32_e32 vcc, v11, v43
	s_waitcnt lgkmcnt(0)
	v_add_f32_e32 v7, v7, v12
	s_waitcnt lgkmcnt(0)
	v_add_f32_e32 v6, v6, v13
	v_cndmask_b32_e32 v11, v42, v11, vcc
	v_cmp_eq_u32_e32 vcc, 0, v8
	v_lshlrev_b32_e32 v11, 2, v11
	v_alignbit_b32 v3, v4, v3, 16
	v_cndmask_b32_e32 v8, v7, v6, vcc
	s_nop 1
	v_mov_b32_dpp v8, v8 quad_perm:[1,0,3,2] row_mask:0xf bank_mask:0xf
	v_alignbit_b32 v4, v5, v4, 16
	v_alignbit_b32 v5, v10, v5, 16
	global_store_dwordx4 v[18:19], v[2:5], off offset:1024
	s_nop 1
	v_cndmask_b32_e32 v2, v6, v7, vcc
	s_waitcnt lgkmcnt(0)
	v_add_f32_e32 v2, v2, v8
	v_cmp_lt_u32_e32 vcc, 15, v79
	s_and_saveexec_b64 s[2:3], vcc
	s_xor_b64 s[2:3], exec, s[2:3]
	s_cbranch_execz .LBB0_5
	v_mul_f32_e32 v1, 0x3fb8aa3b, v2
	v_mul_f32_e32 v2, 0x3e4ccccd, v2
	s_lshr_b32 s6, s8, 2
	v_add_u32_e32 v0, -16, v79
	v_exp_f32_e32 v1, v1
	v_mul_f32_e32 v2, 0x3fb8aa3b, v2
	v_lshrrev_b32_e32 v0, 3, v0
	s_mulk_i32 s6, 0xc0
	v_exp_f32_e32 v2, v2
	s_load_dwordx2 s[4:5], s[0:1], 0x20
	v_add_u32_e32 v0, s6, v0
	s_lshl_b32 s6, s8, 1
	v_add_lshl_u32 v0, v0, v9, 3
	s_and_b32 s6, s6, 6
	v_or3_b32 v0, v0, s6, v67
	v_cvt_f16_f32_e32 v3, v1
	v_lshl_or_b32 v0, v0, 4, v78
	v_cvt_f16_f32_e32 v2, v2
	v_ashrrev_i32_e32 v1, 31, v0
	s_waitcnt lgkmcnt(0)
	v_lshl_add_u64 v[0:1], v[0:1], 1, s[4:5]
	global_store_short v[0:1], v3, off
	global_store_short v[0:1], v2, off offset:16
